# NSA compressed-branch tiles: K fragments in two LDS round trips and V fragments fetched one batch ahead (spare v[230:245]) instead of one round trip per MFMA pair
# baseline (speedup 1.0000x reference)
.LBB0_572:
	v_lshlrev_b32_e32 v202, 10, v3
	v_lshlrev_b32_e32 v203, 4, v198
	v_add3_u32 v69, 0, v202, v203
	ds_read_b128 v[4:7], v69
	ds_read_b128 v[8:11], v69 offset:512
	ds_read_b128 v[230:233], v69 offset:2048
	ds_read_b128 v[234:237], v69 offset:2560
	ds_read_b128 v[238:241], v69 offset:4096
	ds_read_b128 v[242:245], v69 offset:4608
	s_mov_b32 s0, 0xf149f2ca
	v_ashrrev_i32_e32 v182, 3, v68
	s_waitcnt lgkmcnt(5)
	v_mfma_f32_32x32x16_bf16 v[52:67], v[4:7], v[158:161], 0
	s_cmp_lt_i32 s82, 0
	s_waitcnt lgkmcnt(4)
	v_mfma_f32_32x32x16_bf16 v[36:51], v[8:11], v[158:161], 0
	ds_read_b128 v[4:7], v69 offset:6144
	ds_read_b128 v[8:11], v69 offset:6656
	s_waitcnt lgkmcnt(5)
	v_mfma_f32_32x32x16_bf16 v[52:67], v[230:233], v[154:157], v[52:67]
	s_waitcnt lgkmcnt(4)
	v_mfma_f32_32x32x16_bf16 v[36:51], v[234:237], v[154:157], v[36:51]
	s_waitcnt lgkmcnt(3)
	v_mfma_f32_32x32x16_bf16 v[52:67], v[238:241], v[150:153], v[52:67]
	s_waitcnt lgkmcnt(2)
	v_mfma_f32_32x32x16_bf16 v[36:51], v[242:245], v[150:153], v[36:51]
	s_waitcnt lgkmcnt(1)
	v_mfma_f32_32x32x16_bf16 v[52:67], v[4:7], v[146:149], v[52:67]
	s_waitcnt lgkmcnt(0)
	v_mfma_f32_32x32x16_bf16 v[36:51], v[8:11], v[146:149], v[36:51]
	ds_read_b128 v[4:7], v69 offset:16384
	ds_read_b128 v[8:11], v69 offset:16896
	ds_read_b128 v[74:77], v69 offset:18432
	ds_read_b128 v[78:81], v69 offset:18944
	ds_read_b128 v[230:233], v69 offset:20480
	ds_read_b128 v[234:237], v69 offset:20992
	ds_read_b128 v[238:241], v69 offset:22528
	ds_read_b128 v[242:245], v69 offset:23040
	s_waitcnt lgkmcnt(7)
	v_mfma_f32_32x32x16_bf16 v[20:35], v[4:7], v[158:161], 0
	s_waitcnt lgkmcnt(6)
	v_mfma_f32_32x32x16_bf16 v[4:19], v[8:11], v[158:161], 0
	s_waitcnt lgkmcnt(5)
	v_mfma_f32_32x32x16_bf16 v[20:35], v[74:77], v[154:157], v[20:35]
	s_waitcnt lgkmcnt(4)
	v_mfma_f32_32x32x16_bf16 v[4:19], v[78:81], v[154:157], v[4:19]
	s_waitcnt lgkmcnt(3)
	v_mfma_f32_32x32x16_bf16 v[20:35], v[230:233], v[150:153], v[20:35]
	s_waitcnt lgkmcnt(2)
	v_mfma_f32_32x32x16_bf16 v[4:19], v[234:237], v[150:153], v[4:19]
	v_lshlrev_b32_e32 v69, 6, v3
	v_sub_u32_e32 v69, v72, v69
	v_subrev_u32_e32 v72, 31, v69
	v_cmp_lt_i32_e32 vcc, -1, v72
	s_nop 1
	v_cndmask_b32_e32 v52, v195, v52, vcc
	v_cmp_lt_i32_e32 vcc, 15, v72
	s_waitcnt lgkmcnt(1)
	v_mfma_f32_32x32x16_bf16 v[20:35], v[238:241], v[146:149], v[20:35]
	v_cndmask_b32_e32 v53, v195, v53, vcc
	v_cmp_lt_i32_e32 vcc, 31, v72
	v_max3_f32 v69, v52, s0, v53
	s_movk_i32 s0, 0x7f
	v_cndmask_b32_e32 v54, v195, v54, vcc
	v_cmp_lt_i32_e32 vcc, 47, v72
	s_waitcnt lgkmcnt(0)
	v_mfma_f32_32x32x16_bf16 v[4:19], v[242:245], v[146:149], v[4:19]
	v_cndmask_b32_e32 v55, v195, v55, vcc
	v_cmp_lt_i32_e32 vcc, s0, v72
	s_movk_i32 s0, 0x8f
	v_max3_f32 v69, v69, v54, v55
	v_cndmask_b32_e32 v73, v195, v56, vcc
	v_cmp_lt_i32_e32 vcc, s0, v72
	s_movk_i32 s0, 0x9f
	s_nop 0
	v_cndmask_b32_e32 v74, v195, v57, vcc
	v_cmp_lt_i32_e32 vcc, s0, v72
	s_movk_i32 s0, 0xaf
	v_max3_f32 v56, v69, v73, v74
	v_cndmask_b32_e32 v75, v195, v58, vcc
	v_cmp_lt_i32_e32 vcc, s0, v72
	s_movk_i32 s0, 0xff
	s_nop 0
	v_cndmask_b32_e32 v76, v195, v59, vcc
	v_cmp_lt_i32_e32 vcc, s0, v72
	s_movk_i32 s0, 0x10f
	v_max3_f32 v56, v56, v75, v76
	v_cndmask_b32_e32 v77, v195, v60, vcc
	v_cmp_lt_i32_e32 vcc, s0, v72
	s_movk_i32 s0, 0x11f
	s_nop 0
	v_cndmask_b32_e32 v78, v195, v61, vcc
	v_cmp_lt_i32_e32 vcc, s0, v72
	s_movk_i32 s0, 0x12f
	v_max3_f32 v56, v56, v77, v78
	v_cndmask_b32_e32 v79, v195, v62, vcc
	v_cmp_lt_i32_e32 vcc, s0, v72
	s_movk_i32 s0, 0x17f
	s_nop 0
	v_cndmask_b32_e32 v80, v195, v63, vcc
	v_cmp_lt_i32_e32 vcc, s0, v72
	s_movk_i32 s0, 0x18f
	v_max3_f32 v56, v56, v79, v80
	v_cndmask_b32_e32 v81, v195, v64, vcc
	v_cmp_lt_i32_e32 vcc, s0, v72
	s_movk_i32 s0, 0x19f
	s_nop 0
	v_cndmask_b32_e32 v82, v195, v65, vcc
	v_cmp_lt_i32_e32 vcc, s0, v72
	s_movk_i32 s0, 0x1af
	v_max3_f32 v56, v56, v81, v82
	v_cndmask_b32_e32 v83, v195, v66, vcc
	v_cmp_lt_i32_e32 vcc, s0, v72
	s_movk_i32 s0, 0x1ff
	s_nop 0
	v_cndmask_b32_e32 v84, v195, v67, vcc
	v_cmp_lt_i32_e32 vcc, s0, v72
	s_movk_i32 s0, 0x20f
	v_max3_f32 v56, v56, v83, v84
	v_cndmask_b32_e32 v36, v195, v36, vcc
	v_cmp_lt_i32_e32 vcc, s0, v72
	s_movk_i32 s0, 0x21f
	s_nop 0
	v_cndmask_b32_e32 v37, v195, v37, vcc
	v_cmp_lt_i32_e32 vcc, s0, v72
	s_movk_i32 s0, 0x22f
	v_max3_f32 v56, v56, v36, v37
	v_cndmask_b32_e32 v38, v195, v38, vcc
	v_cmp_lt_i32_e32 vcc, s0, v72
	s_movk_i32 s0, 0x27f
	s_nop 0
	v_cndmask_b32_e32 v39, v195, v39, vcc
	v_cmp_lt_i32_e32 vcc, s0, v72
	s_movk_i32 s0, 0x28f
	v_max3_f32 v56, v56, v38, v39
	v_cndmask_b32_e32 v40, v195, v40, vcc
	v_cmp_lt_i32_e32 vcc, s0, v72
	s_movk_i32 s0, 0x29f
	s_nop 0
	v_cndmask_b32_e32 v41, v195, v41, vcc
	v_cmp_lt_i32_e32 vcc, s0, v72
	s_movk_i32 s0, 0x2af
	v_max3_f32 v56, v56, v40, v41
	v_cndmask_b32_e32 v42, v195, v42, vcc
	v_cmp_lt_i32_e32 vcc, s0, v72
	s_movk_i32 s0, 0x2ff
	s_nop 0
	v_cndmask_b32_e32 v43, v195, v43, vcc
	v_cmp_lt_i32_e32 vcc, s0, v72
	s_movk_i32 s0, 0x30f
	v_max3_f32 v56, v56, v42, v43
	v_cndmask_b32_e32 v44, v195, v44, vcc
	v_cmp_lt_i32_e32 vcc, s0, v72
	s_movk_i32 s0, 0x31f
	s_nop 0
	v_cndmask_b32_e32 v45, v195, v45, vcc
	v_cmp_lt_i32_e32 vcc, s0, v72
	s_movk_i32 s0, 0x32f
	v_max3_f32 v56, v56, v44, v45
	v_cndmask_b32_e32 v46, v195, v46, vcc
	v_cmp_lt_i32_e32 vcc, s0, v72
	s_movk_i32 s0, 0x37f
	s_nop 0
	v_cndmask_b32_e32 v47, v195, v47, vcc
	v_cmp_lt_i32_e32 vcc, s0, v72
	s_movk_i32 s0, 0x38f
	v_max3_f32 v56, v56, v46, v47
	v_cndmask_b32_e32 v48, v195, v48, vcc
	v_cmp_lt_i32_e32 vcc, s0, v72
	s_movk_i32 s0, 0x39f
	s_nop 0
	v_cndmask_b32_e32 v49, v195, v49, vcc
	v_cmp_lt_i32_e32 vcc, s0, v72
	s_movk_i32 s0, 0x3af
	v_max3_f32 v56, v56, v48, v49
	v_cndmask_b32_e32 v50, v195, v50, vcc
	v_cmp_lt_i32_e32 vcc, s0, v72
	s_movk_i32 s0, 0x40f
	s_nop 0
	v_cndmask_b32_e32 v51, v195, v51, vcc
	v_cmp_lt_i32_e32 vcc, s39, v72
	v_max3_f32 v56, v56, v50, v51
	s_nop 0
	v_cndmask_b32_e32 v85, v195, v20, vcc
	v_cmp_lt_i32_e32 vcc, s0, v72
	s_movk_i32 s0, 0x41f
	s_nop 0
	v_cndmask_b32_e32 v86, v195, v21, vcc
	v_cmp_lt_i32_e32 vcc, s0, v72
	s_movk_i32 s0, 0x42f
	v_max3_f32 v20, v56, v85, v86
	v_cndmask_b32_e32 v87, v195, v22, vcc
	v_cmp_lt_i32_e32 vcc, s0, v72
	s_movk_i32 s0, 0x47f
	s_nop 0
	v_cndmask_b32_e32 v88, v195, v23, vcc
	v_cmp_lt_i32_e32 vcc, s0, v72
	s_movk_i32 s0, 0x48f
	v_max3_f32 v20, v20, v87, v88
	v_cndmask_b32_e32 v89, v195, v24, vcc
	v_cmp_lt_i32_e32 vcc, s0, v72
	s_movk_i32 s0, 0x49f
	s_nop 0
	v_cndmask_b32_e32 v90, v195, v25, vcc
	v_cmp_lt_i32_e32 vcc, s0, v72
	s_movk_i32 s0, 0x4af
	v_max3_f32 v20, v20, v89, v90
	v_cndmask_b32_e32 v91, v195, v26, vcc
	v_cmp_lt_i32_e32 vcc, s0, v72
	s_movk_i32 s0, 0x4ff
	s_nop 0
	v_cndmask_b32_e32 v92, v195, v27, vcc
	v_cmp_lt_i32_e32 vcc, s0, v72
	s_movk_i32 s0, 0x50f
	v_max3_f32 v20, v20, v91, v92
	v_cndmask_b32_e32 v93, v195, v28, vcc
	v_cmp_lt_i32_e32 vcc, s0, v72
	s_movk_i32 s0, 0x51f
	s_nop 0
	v_cndmask_b32_e32 v94, v195, v29, vcc
	v_cmp_lt_i32_e32 vcc, s0, v72
	s_movk_i32 s0, 0x52f
	v_max3_f32 v20, v20, v93, v94
	v_cndmask_b32_e32 v95, v195, v30, vcc
	v_cmp_lt_i32_e32 vcc, s0, v72
	s_movk_i32 s0, 0x57f
	s_nop 0
	v_cndmask_b32_e32 v96, v195, v31, vcc
	v_cmp_lt_i32_e32 vcc, s0, v72
	s_movk_i32 s0, 0x58f
	v_max3_f32 v20, v20, v95, v96
	v_cndmask_b32_e32 v97, v195, v32, vcc
	v_cmp_lt_i32_e32 vcc, s0, v72
	s_movk_i32 s0, 0x59f
	s_nop 0
	v_cndmask_b32_e32 v98, v195, v33, vcc
	v_cmp_lt_i32_e32 vcc, s0, v72
	s_movk_i32 s0, 0x5af
	v_max3_f32 v20, v20, v97, v98
	v_cndmask_b32_e32 v99, v195, v34, vcc
	v_cmp_lt_i32_e32 vcc, s0, v72
	s_movk_i32 s0, 0x5ff
	s_nop 0
	v_cndmask_b32_e32 v100, v195, v35, vcc
	v_cmp_lt_i32_e32 vcc, s0, v72
	s_movk_i32 s0, 0x60f
	v_max3_f32 v20, v20, v99, v100
	v_cndmask_b32_e32 v101, v195, v4, vcc
	v_cmp_lt_i32_e32 vcc, s0, v72
	s_movk_i32 s0, 0x61f
	s_nop 0
	v_cndmask_b32_e32 v102, v195, v5, vcc
	v_cmp_lt_i32_e32 vcc, s0, v72
	s_movk_i32 s0, 0x62f
	v_max3_f32 v4, v20, v101, v102
	v_cndmask_b32_e32 v103, v195, v6, vcc
	v_cmp_lt_i32_e32 vcc, s0, v72
	s_movk_i32 s0, 0x67f
	s_nop 0
	v_cndmask_b32_e32 v104, v195, v7, vcc
	v_cmp_lt_i32_e32 vcc, s0, v72
	s_movk_i32 s0, 0x68f
	v_max3_f32 v4, v4, v103, v104
	v_cndmask_b32_e32 v58, v195, v8, vcc
	v_cmp_lt_i32_e32 vcc, s0, v72
	s_movk_i32 s0, 0x69f
	s_nop 0
	v_cndmask_b32_e32 v59, v195, v9, vcc
	v_cmp_lt_i32_e32 vcc, s0, v72
	s_movk_i32 s0, 0x6af
	v_max3_f32 v4, v4, v58, v59
	v_cndmask_b32_e32 v56, v195, v10, vcc
	v_cmp_lt_i32_e32 vcc, s0, v72
	s_movk_i32 s0, 0x6ff
	s_nop 0
	v_cndmask_b32_e32 v57, v195, v11, vcc
	v_cmp_lt_i32_e32 vcc, s0, v72
	s_movk_i32 s0, 0x70f
	v_max3_f32 v4, v4, v56, v57
	v_cndmask_b32_e32 v62, v195, v12, vcc
	v_cmp_lt_i32_e32 vcc, s0, v72
	s_movk_i32 s0, 0x71f
	s_nop 0
	v_cndmask_b32_e32 v63, v195, v13, vcc
	v_cmp_lt_i32_e32 vcc, s0, v72
	s_movk_i32 s0, 0x72f
	v_max3_f32 v4, v4, v62, v63
	v_cndmask_b32_e32 v60, v195, v14, vcc
	v_cmp_lt_i32_e32 vcc, s0, v72
	s_movk_i32 s0, 0x77f
	s_nop 0
	v_cndmask_b32_e32 v61, v195, v15, vcc
	v_cmp_lt_i32_e32 vcc, s0, v72
	s_movk_i32 s0, 0x78f
	v_max3_f32 v4, v4, v60, v61
	v_cndmask_b32_e32 v69, v195, v16, vcc
	v_cmp_lt_i32_e32 vcc, s0, v72
	s_movk_i32 s0, 0x79f
	s_nop 0
	v_cndmask_b32_e32 v66, v195, v17, vcc
	v_cmp_lt_i32_e32 vcc, s0, v72
	s_movk_i32 s0, 0x7af
	v_max3_f32 v4, v4, v69, v66
	v_cndmask_b32_e32 v65, v195, v18, vcc
	v_cmp_lt_i32_e32 vcc, s0, v72
	s_mov_b32 s0, 0xefa18f08
	s_nop 0
	v_cndmask_b32_e32 v64, v195, v19, vcc
	v_max3_f32 v4, v4, v65, v64
	v_mov_b32_e32 v5, v4
	s_nop 1
	v_permlane32_swap_b32_e32 v4, v5
	v_max3_f32 v67, v4, v5, s0
	v_sub_f32_e32 v4, v52, v67
	v_exp_f32_e32 v4, v4
	v_sub_f32_e32 v5, v53, v67
	v_exp_f32_e32 v5, v5
	v_sub_f32_e32 v9, v73, v67
	v_add_f32_e32 v6, 0, v4
	v_exp_f32_e32 v10, v9
	v_add_f32_e32 v7, v5, v6
	v_sub_f32_e32 v6, v54, v67
	v_exp_f32_e32 v6, v6
	v_sub_f32_e32 v9, v74, v67
	v_exp_f32_e32 v11, v9
	v_sub_f32_e32 v13, v77, v67
	v_add_f32_e32 v8, v6, v7
	v_sub_f32_e32 v7, v55, v67
	v_exp_f32_e32 v7, v7
	v_exp_f32_e32 v14, v13
	v_sub_f32_e32 v13, v78, v67
	v_exp_f32_e32 v15, v13
	v_add_f32_e32 v8, v7, v8
	v_add_f32_e32 v8, v10, v8
	v_add_f32_e32 v9, v11, v8
	v_sub_f32_e32 v8, v75, v67
	v_exp_f32_e32 v8, v8
	v_sub_f32_e32 v17, v81, v67
	v_exp_f32_e32 v18, v17
	v_sub_f32_e32 v17, v82, v67
	v_add_f32_e32 v12, v8, v9
	v_sub_f32_e32 v9, v76, v67
	v_exp_f32_e32 v9, v9
	v_exp_f32_e32 v19, v17
	v_sub_f32_e32 v21, v36, v67
	v_exp_f32_e32 v22, v21
	v_add_f32_e32 v12, v9, v12
	v_add_f32_e32 v12, v14, v12
	v_add_f32_e32 v13, v15, v12
	v_sub_f32_e32 v12, v79, v67
	v_exp_f32_e32 v12, v12
	v_sub_f32_e32 v21, v37, v67
	v_exp_f32_e32 v23, v21
	v_sub_f32_e32 v25, v40, v67
	v_add_f32_e32 v16, v12, v13
	v_sub_f32_e32 v13, v80, v67
	v_exp_f32_e32 v13, v13
	v_exp_f32_e32 v26, v25
	v_sub_f32_e32 v25, v41, v67
	v_exp_f32_e32 v27, v25
	v_add_f32_e32 v16, v13, v16
	v_add_f32_e32 v16, v18, v16
	v_add_f32_e32 v17, v19, v16
	v_sub_f32_e32 v16, v83, v67
	v_exp_f32_e32 v16, v16
	v_sub_f32_e32 v29, v44, v67
	v_exp_f32_e32 v30, v29
	v_sub_f32_e32 v29, v45, v67
	v_add_f32_e32 v20, v16, v17
	v_sub_f32_e32 v17, v84, v67
	v_exp_f32_e32 v17, v17
	v_exp_f32_e32 v31, v29
	v_sub_f32_e32 v33, v48, v67
	v_exp_f32_e32 v34, v33
	v_add_f32_e32 v20, v17, v20
	v_add_f32_e32 v20, v22, v20
	v_add_f32_e32 v21, v23, v20
	v_sub_f32_e32 v20, v38, v67
	v_exp_f32_e32 v20, v20
	v_sub_f32_e32 v33, v49, v67
	v_exp_f32_e32 v35, v33
	v_sub_f32_e32 v37, v85, v67
	v_add_f32_e32 v24, v20, v21
	v_sub_f32_e32 v21, v39, v67
	v_exp_f32_e32 v21, v21
	v_exp_f32_e32 v38, v37
	v_sub_f32_e32 v37, v86, v67
	v_exp_f32_e32 v39, v37
	v_add_f32_e32 v24, v21, v24
	v_add_f32_e32 v24, v26, v24
	v_add_f32_e32 v25, v27, v24
	v_sub_f32_e32 v24, v42, v67
	v_exp_f32_e32 v24, v24
	v_sub_f32_e32 v41, v89, v67
	v_exp_f32_e32 v42, v41
	v_sub_f32_e32 v41, v90, v67
	v_add_f32_e32 v28, v24, v25
	v_sub_f32_e32 v25, v43, v67
	v_exp_f32_e32 v25, v25
	v_exp_f32_e32 v43, v41
	v_sub_f32_e32 v45, v93, v67
	v_sub_f32_e32 v49, v97, v67
	v_add_f32_e32 v28, v25, v28
	v_add_f32_e32 v28, v30, v28
	v_add_f32_e32 v29, v31, v28
	v_sub_f32_e32 v28, v46, v67
	v_exp_f32_e32 v28, v28
	v_exp_f32_e32 v46, v45
	v_sub_f32_e32 v45, v94, v67
	v_sub_f32_e32 v53, v101, v67
	v_add_f32_e32 v32, v28, v29
	v_sub_f32_e32 v29, v47, v67
	v_exp_f32_e32 v29, v29
	v_exp_f32_e32 v47, v45
	v_exp_f32_e32 v54, v53
	v_sub_f32_e32 v53, v102, v67
	v_add_f32_e32 v32, v29, v32
	v_add_f32_e32 v32, v34, v32
	v_add_f32_e32 v33, v35, v32
	v_sub_f32_e32 v32, v50, v67
	v_exp_f32_e32 v32, v32
	v_exp_f32_e32 v50, v49
	v_sub_f32_e32 v49, v98, v67
	v_exp_f32_e32 v55, v53
	v_add_f32_e32 v36, v32, v33
	v_sub_f32_e32 v33, v51, v67
	v_exp_f32_e32 v33, v33
	v_exp_f32_e32 v51, v49
	v_sub_f32_e32 v58, v58, v67
	v_exp_f32_e32 v58, v58
	v_add_f32_e32 v36, v33, v36
	v_add_f32_e32 v36, v38, v36
	v_add_f32_e32 v37, v39, v36
	v_sub_f32_e32 v36, v87, v67
	v_exp_f32_e32 v36, v36
	v_sub_f32_e32 v59, v59, v67
	v_exp_f32_e32 v59, v59
	v_sub_f32_e32 v56, v56, v67
	v_add_f32_e32 v40, v36, v37
	v_sub_f32_e32 v37, v88, v67
	v_exp_f32_e32 v37, v37
	v_exp_f32_e32 v56, v56
	v_sub_f32_e32 v57, v57, v67
	v_exp_f32_e32 v57, v57
	v_add_f32_e32 v40, v37, v40
	v_add_f32_e32 v40, v42, v40
	v_add_f32_e32 v41, v43, v40
	v_sub_f32_e32 v40, v91, v67
	v_exp_f32_e32 v40, v40
	v_sub_f32_e32 v62, v62, v67
	v_exp_f32_e32 v62, v62
	v_sub_f32_e32 v63, v63, v67
	v_add_f32_e32 v44, v40, v41
	v_sub_f32_e32 v41, v92, v67
	v_exp_f32_e32 v41, v41
	v_exp_f32_e32 v63, v63
	v_sub_f32_e32 v60, v60, v67
	v_exp_f32_e32 v60, v60
	v_add_f32_e32 v44, v41, v44
	v_add_f32_e32 v44, v46, v44
	v_add_f32_e32 v45, v47, v44
	v_sub_f32_e32 v44, v95, v67
	v_exp_f32_e32 v44, v44
	v_sub_f32_e32 v61, v61, v67
	v_exp_f32_e32 v61, v61
	v_sub_f32_e32 v69, v69, v67
	v_add_f32_e32 v48, v44, v45
	v_sub_f32_e32 v45, v96, v67
	v_exp_f32_e32 v45, v45
	v_sub_f32_e32 v66, v66, v67
	v_sub_f32_e32 v65, v65, v67
	v_sub_f32_e32 v64, v64, v67
	v_add_f32_e32 v48, v45, v48
	v_add_f32_e32 v48, v50, v48
	v_add_f32_e32 v49, v51, v48
	v_sub_f32_e32 v48, v99, v67
	v_exp_f32_e32 v48, v48
	s_nop 0
	v_add_f32_e32 v52, v48, v49
	v_sub_f32_e32 v49, v100, v67
	v_exp_f32_e32 v49, v49
	s_nop 0
	v_add_f32_e32 v52, v49, v52
	v_add_f32_e32 v52, v54, v52
	v_add_f32_e32 v53, v55, v52
	v_sub_f32_e32 v52, v103, v67
	v_exp_f32_e32 v52, v52
	s_nop 0
	v_add_f32_e32 v72, v52, v53
	v_sub_f32_e32 v53, v104, v67
	v_exp_f32_e32 v53, v53
	v_exp_f32_e32 v67, v64
	v_add_f32_e32 v72, v53, v72
	v_add_f32_e32 v72, v58, v72
	v_add_f32_e32 v72, v59, v72
	v_add_f32_e32 v72, v56, v72
	v_add_f32_e32 v72, v57, v72
	v_add_f32_e32 v72, v62, v72
	v_add_f32_e32 v72, v63, v72
	v_add_f32_e32 v72, v60, v72
	v_add_f32_e32 v73, v61, v72
	v_exp_f32_e32 v72, v69
	s_nop 0
	v_add_f32_e32 v69, v72, v73
	v_exp_f32_e32 v73, v66
	v_exp_f32_e32 v66, v65
	v_add_f32_e32 v69, v73, v69
	v_add_f32_e32 v65, v66, v69
	v_add_f32_e32 v64, v67, v65
	v_mov_b32_e32 v65, v64
	s_nop 1
	v_permlane32_swap_b32_e32 v64, v65
	v_add_f32_e32 v64, v64, v65
	v_div_scale_f32 v65, s[2:3], v64, v64, 1.0
	v_rcp_f32_e32 v69, v65
	v_cmp_lt_f32_e64 s[0:1], 0, v64
	v_fma_f32 v74, -v65, v69, 1.0
	v_fmac_f32_e32 v69, v74, v69
	v_div_scale_f32 v74, vcc, 1.0, v64, 1.0
	v_mul_f32_e32 v75, v74, v69
	v_fma_f32 v76, -v65, v75, v74
	v_fmac_f32_e32 v75, v76, v69
	v_fma_f32 v65, -v65, v75, v74
	v_div_fmas_f32 v65, v65, v69, v75
	v_and_b32_e32 v69, 64, v212
	v_div_fixup_f32 v64, v65, v64, 1.0
	v_xor_b32_e32 v65, 32, v212
	v_add_u32_e32 v69, 64, v69
	v_cmp_lt_i32_e32 vcc, v65, v69
	v_cndmask_b32_e64 v76, 0, v64, s[0:1]
	v_add_u32_e32 v64, s12, v71
	v_cndmask_b32_e32 v65, v212, v65, vcc
	v_lshlrev_b32_e32 v77, 2, v65
	v_pk_mul_f32 v[6:7], v[6:7], v[76:77] op_sel_hi:[1,0]
	ds_bpermute_b32 v74, v77, v7
	v_mul_lo_u32 v64, v64, s64
	v_lshlrev_b32_e32 v69, 2, v3
	v_add3_u32 v88, s33, v64, v69
	v_pk_mul_f32 v[64:65], v[4:5], v[76:77] op_sel_hi:[1,0]
	v_cmp_gt_u32_e32 vcc, 32, v68
	v_pk_mul_f32 v[4:5], v[70:71], v[64:65] op_sel_hi:[0,1]
	v_add_f32_e32 v75, v6, v7
	v_add_f32_e32 v64, v64, v65
	v_add_f32_e32 v64, v64, v75
	s_waitcnt lgkmcnt(0)
	v_cndmask_b32_e64 v65, v74, 0, vcc
	v_pk_mul_f32 v[8:9], v[8:9], v[76:77] op_sel_hi:[1,0]
	v_add_f32_e32 v64, v65, v64
	ds_bpermute_b32 v65, v77, v9
	v_pk_mul_f32 v[10:11], v[10:11], v[76:77] op_sel_hi:[1,0]
	v_add_f32_e32 v75, v8, v9
	v_pk_mul_f32 v[78:79], v[70:71], v[10:11] op_sel_hi:[0,1]
	v_add_f32_e32 v10, v10, v11
	v_add_f32_e32 v10, v10, v75
	s_waitcnt lgkmcnt(0)
	v_cndmask_b32_e32 v11, v65, v74, vcc
	v_add_f32_e32 v10, v11, v10
	ds_write2_b32 v88, v64, v10 offset1:2
	v_pk_mul_f32 v[10:11], v[12:13], v[76:77] op_sel_hi:[1,0]
	ds_bpermute_b32 v12, v77, v11
	v_add_f32_e32 v13, v10, v11
	v_pk_mul_f32 v[84:85], v[70:71], v[10:11] op_sel_hi:[0,1]
	v_pk_mul_f32 v[10:11], v[16:17], v[76:77] op_sel_hi:[1,0]
	v_pk_mul_f32 v[80:81], v[70:71], v[8:9] op_sel_hi:[0,1]
	v_pk_mul_f32 v[8:9], v[14:15], v[76:77] op_sel_hi:[1,0]
	ds_bpermute_b32 v14, v77, v11
	v_pk_mul_f32 v[82:83], v[70:71], v[8:9] op_sel_hi:[0,1]
	v_add_f32_e32 v8, v8, v9
	v_add_f32_e32 v8, v8, v13
	s_waitcnt lgkmcnt(1)
	v_cndmask_b32_e32 v9, v12, v65, vcc
	v_add_f32_e32 v13, v9, v8
	v_pk_mul_f32 v[8:9], v[18:19], v[76:77] op_sel_hi:[1,0]
	v_add_f32_e32 v15, v10, v11
	v_pk_mul_f32 v[86:87], v[70:71], v[10:11] op_sel_hi:[0,1]
	v_pk_mul_f32 v[10:11], v[20:21], v[76:77] op_sel_hi:[1,0]
	v_pk_mul_f32 v[18:19], v[70:71], v[8:9] op_sel_hi:[0,1]
	v_add_f32_e32 v8, v8, v9
	s_waitcnt lgkmcnt(0)
	v_cndmask_b32_e32 v9, v14, v12, vcc
	ds_bpermute_b32 v12, v77, v11
	v_add_f32_e32 v8, v8, v15
	v_add_f32_e32 v8, v9, v8
	ds_write2_b32 v88, v13, v8 offset0:4 offset1:6
	v_pk_mul_f32 v[8:9], v[22:23], v[76:77] op_sel_hi:[1,0]
	v_add_f32_e32 v13, v10, v11
	v_pk_mul_f32 v[20:21], v[70:71], v[10:11] op_sel_hi:[0,1]
	v_pk_mul_f32 v[10:11], v[24:25], v[76:77] op_sel_hi:[1,0]
	v_pk_mul_f32 v[22:23], v[70:71], v[8:9] op_sel_hi:[0,1]
	v_add_f32_e32 v8, v8, v9
	s_waitcnt lgkmcnt(1)
	v_cndmask_b32_e32 v9, v12, v14, vcc
	ds_bpermute_b32 v14, v77, v11
	v_add_f32_e32 v8, v8, v13
	v_add_f32_e32 v13, v8, v9
	v_pk_mul_f32 v[8:9], v[26:27], v[76:77] op_sel_hi:[1,0]
	v_add_f32_e32 v15, v10, v11
	v_pk_mul_f32 v[24:25], v[70:71], v[10:11] op_sel_hi:[0,1]
	v_pk_mul_f32 v[10:11], v[28:29], v[76:77] op_sel_hi:[1,0]
	v_pk_mul_f32 v[26:27], v[70:71], v[8:9] op_sel_hi:[0,1]
	v_add_f32_e32 v8, v8, v9
	s_waitcnt lgkmcnt(0)
	v_cndmask_b32_e32 v9, v14, v12, vcc
	ds_bpermute_b32 v12, v77, v11
	v_add_f32_e32 v8, v8, v15
	v_add_f32_e32 v8, v8, v9
	ds_write2_b32 v88, v13, v8 offset0:8 offset1:10
	v_pk_mul_f32 v[8:9], v[30:31], v[76:77] op_sel_hi:[1,0]
	v_add_f32_e32 v13, v10, v11
	v_pk_mul_f32 v[28:29], v[70:71], v[10:11] op_sel_hi:[0,1]
	v_pk_mul_f32 v[10:11], v[32:33], v[76:77] op_sel_hi:[1,0]
	v_pk_mul_f32 v[30:31], v[70:71], v[8:9] op_sel_hi:[0,1]
	v_add_f32_e32 v8, v8, v9
	s_waitcnt lgkmcnt(1)
	v_cndmask_b32_e32 v9, v12, v14, vcc
	ds_bpermute_b32 v14, v77, v11
	v_add_f32_e32 v8, v8, v13
	v_add_f32_e32 v13, v8, v9
	v_pk_mul_f32 v[8:9], v[34:35], v[76:77] op_sel_hi:[1,0]
	v_add_f32_e32 v15, v10, v11
	v_pk_mul_f32 v[34:35], v[70:71], v[8:9] op_sel_hi:[0,1]
	v_add_f32_e32 v8, v8, v9
	v_add_f32_e32 v8, v8, v15
	s_waitcnt lgkmcnt(0)
	v_cndmask_b32_e32 v9, v14, v12, vcc
	v_add_f32_e32 v8, v8, v9
	ds_write2_b32 v88, v13, v8 offset0:12 offset1:14
	v_pk_mul_f32 v[12:13], v[36:37], v[76:77] op_sel_hi:[1,0]
	ds_bpermute_b32 v36, v77, v13
	v_pk_mul_f32 v[16:17], v[40:41], v[76:77] op_sel_hi:[1,0]
	ds_bpermute_b32 v40, v77, v17
	v_pk_mul_f32 v[32:33], v[70:71], v[10:11] op_sel_hi:[0,1]
	v_pk_mul_f32 v[10:11], v[38:39], v[76:77] op_sel_hi:[1,0]
	v_add_f32_e32 v15, v12, v13
	v_pk_mul_f32 v[8:9], v[70:71], v[10:11] op_sel_hi:[0,1]
	v_add_f32_e32 v10, v10, v11
	v_add_f32_e32 v10, v10, v15
	s_waitcnt lgkmcnt(1)
	v_cndmask_b32_e32 v11, v36, v14, vcc
	v_pk_mul_f32 v[14:15], v[42:43], v[76:77] op_sel_hi:[1,0]
	v_add_f32_e32 v37, v10, v11
	v_pk_mul_f32 v[10:11], v[70:71], v[12:13] op_sel_hi:[0,1]
	v_pk_mul_f32 v[12:13], v[70:71], v[14:15] op_sel_hi:[0,1]
	v_add_f32_e32 v38, v16, v17
	v_add_f32_e32 v14, v14, v15
	v_add_f32_e32 v14, v14, v38
	s_waitcnt lgkmcnt(0)
	v_cndmask_b32_e32 v15, v40, v36, vcc
	v_pk_mul_f32 v[38:39], v[44:45], v[76:77] op_sel_hi:[1,0]
	v_add_f32_e32 v14, v14, v15
	ds_bpermute_b32 v41, v77, v39
	ds_write2_b32 v88, v37, v14 offset0:16 offset1:18
	v_pk_mul_f32 v[36:37], v[46:47], v[76:77] op_sel_hi:[1,0]
	v_pk_mul_f32 v[14:15], v[70:71], v[16:17] op_sel_hi:[0,1]
	v_pk_mul_f32 v[16:17], v[70:71], v[36:37] op_sel_hi:[0,1]
	v_add_f32_e32 v42, v38, v39
	v_add_f32_e32 v36, v36, v37
	v_pk_mul_f32 v[64:65], v[70:71], v[38:39] op_sel_hi:[0,1]
	v_pk_mul_f32 v[38:39], v[48:49], v[76:77] op_sel_hi:[1,0]
	v_add_f32_e32 v36, v36, v42
	ds_bpermute_b32 v42, v77, v39
	s_waitcnt lgkmcnt(2)
	v_cndmask_b32_e32 v37, v41, v40, vcc
	v_add_f32_e32 v40, v36, v37
	v_pk_mul_f32 v[36:37], v[50:51], v[76:77] op_sel_hi:[1,0]
	v_add_f32_e32 v43, v38, v39
	v_pk_mul_f32 v[50:51], v[70:71], v[36:37] op_sel_hi:[0,1]
	v_add_f32_e32 v36, v36, v37
	v_add_f32_e32 v36, v36, v43
	s_waitcnt lgkmcnt(0)
	v_cndmask_b32_e32 v37, v42, v41, vcc
	v_add_f32_e32 v36, v36, v37
	v_pk_mul_f32 v[74:75], v[70:71], v[38:39] op_sel_hi:[0,1]
	v_pk_mul_f32 v[38:39], v[52:53], v[76:77] op_sel_hi:[1,0]
	ds_write2_b32 v88, v40, v36 offset0:20 offset1:22
	ds_bpermute_b32 v40, v77, v39
	v_pk_mul_f32 v[36:37], v[54:55], v[76:77] op_sel_hi:[1,0]
	v_add_f32_e32 v41, v38, v39
	v_pk_mul_f32 v[52:53], v[70:71], v[38:39] op_sel_hi:[0,1]
	v_pk_mul_f32 v[38:39], v[56:57], v[76:77] op_sel_hi:[1,0]
	v_pk_mul_f32 v[54:55], v[70:71], v[36:37] op_sel_hi:[0,1]
	v_add_f32_e32 v36, v36, v37
	s_waitcnt lgkmcnt(0)
	v_cndmask_b32_e32 v37, v40, v42, vcc
	ds_bpermute_b32 v42, v77, v39
	v_add_f32_e32 v36, v36, v41
	v_add_f32_e32 v41, v36, v37
	v_pk_mul_f32 v[36:37], v[58:59], v[76:77] op_sel_hi:[1,0]
	v_add_f32_e32 v43, v38, v39
	v_pk_mul_f32 v[56:57], v[70:71], v[38:39] op_sel_hi:[0,1]
	v_pk_mul_f32 v[38:39], v[60:61], v[76:77] op_sel_hi:[1,0]
	v_pk_mul_f32 v[58:59], v[70:71], v[36:37] op_sel_hi:[0,1]
	v_add_f32_e32 v36, v36, v37
	s_waitcnt lgkmcnt(0)
	v_cndmask_b32_e32 v37, v42, v40, vcc
	ds_bpermute_b32 v40, v77, v39
	v_add_f32_e32 v36, v36, v43
	v_add_f32_e32 v36, v36, v37
	ds_write2_b32 v88, v41, v36 offset0:24 offset1:26
	v_pk_mul_f32 v[36:37], v[62:63], v[76:77] op_sel_hi:[1,0]
	v_add_f32_e32 v41, v38, v39
	v_pk_mul_f32 v[60:61], v[70:71], v[38:39] op_sel_hi:[0,1]
	v_pk_mul_f32 v[38:39], v[66:67], v[76:77] op_sel_hi:[1,0]
	v_pk_mul_f32 v[62:63], v[70:71], v[36:37] op_sel_hi:[0,1]
	v_add_f32_e32 v36, v36, v37
	s_waitcnt lgkmcnt(1)
	v_cndmask_b32_e32 v37, v40, v42, vcc
	ds_bpermute_b32 v42, v77, v39
	v_add_f32_e32 v36, v36, v41
	v_add_f32_e32 v41, v36, v37
	v_pk_mul_f32 v[36:37], v[72:73], v[76:77] op_sel_hi:[1,0]
	v_add_f32_e32 v43, v38, v39
	v_pk_mul_f32 v[72:73], v[70:71], v[36:37] op_sel_hi:[0,1]
	v_add_f32_e32 v36, v36, v37
	v_cvt_pk_bf16_f32 v78, v78, v79
	v_cvt_pk_bf16_f32 v79, v80, v81
	v_cvt_pk_bf16_f32 v80, v82, v83
	v_cvt_pk_bf16_f32 v82, v18, v19
	v_lshlrev_b32_e32 v18, 1, v68
	v_bfe_u32 v19, v68, 2, 2
	s_mov_b32 s0, 0x3fffffc
	v_add_f32_e32 v36, v36, v43
	s_waitcnt lgkmcnt(0)
	v_cndmask_b32_e32 v37, v42, v40, vcc
	v_and_b32_e32 v204, 32, v18
	v_and_or_b32 v19, v182, s0, v19
	v_add_f32_e32 v36, v36, v37
	v_add_u32_e32 v18, 0, v204
	v_lshlrev_b32_e32 v205, 6, v19
	v_pk_mul_f32 v[6:7], v[70:71], v[6:7] op_sel_hi:[0,1]
	ds_write2_b32 v88, v41, v36 offset0:28 offset1:30
	v_pk_mul_f32 v[66:67], v[70:71], v[38:39] op_sel_hi:[0,1]
	v_add3_u32 v70, v18, v201, v205
	v_add3_u32 v229, v18, v201, v205
	v_cvt_pk_bf16_f32 v81, v84, v85
	v_cvt_pk_bf16_f32 v83, v86, v87
	v_cvt_pk_bf16_f32 v84, v22, v23
	v_cvt_pk_bf16_f32 v85, v20, v21
	v_cvt_pk_bf16_f32 v87, v24, v25
	ds_read_b64_tr_b16 v[230:231], v70 offset:8192
	ds_read_b64_tr_b16 v[232:233], v70 offset:8704
	ds_read_b64_tr_b16 v[234:235], v70 offset:12288
	ds_read_b64_tr_b16 v[236:237], v70 offset:12800
	ds_read_b64_tr_b16 v[238:239], v70 offset:9216
	ds_read_b64_tr_b16 v[240:241], v70 offset:9728
	ds_read_b64_tr_b16 v[242:243], v70 offset:13312
	ds_read_b64_tr_b16 v[244:245], v70 offset:13824
	v_cvt_pk_bf16_f32 v76, v4, v5
	v_cvt_pk_bf16_f32 v77, v6, v7
	v_cvt_pk_bf16_f32 v86, v26, v27
	v_cvt_pk_bf16_f32 v4, v30, v31
	v_cvt_pk_bf16_f32 v5, v28, v29
	v_cvt_pk_bf16_f32 v6, v34, v35
	v_cvt_pk_bf16_f32 v7, v32, v33
	s_waitcnt lgkmcnt(6)
	v_mfma_f32_32x32x16_bf16 v[34:49], v[230:233], v[76:79], 0
	s_waitcnt lgkmcnt(4)
	v_mfma_f32_32x32x16_bf16 v[18:33], v[234:237], v[76:79], 0
	ds_read_b64_tr_b16 v[230:231], v70 offset:10240
	ds_read_b64_tr_b16 v[232:233], v70 offset:10752
	ds_read_b64_tr_b16 v[234:235], v70 offset:14336
	ds_read_b64_tr_b16 v[236:237], v70 offset:14848
	s_waitcnt lgkmcnt(6)
	v_mfma_f32_32x32x16_bf16 v[34:49], v[238:241], v[80:83], v[34:49]
	s_waitcnt lgkmcnt(4)
	v_mfma_f32_32x32x16_bf16 v[18:33], v[242:245], v[80:83], v[18:33]
	ds_read_b64_tr_b16 v[238:239], v70 offset:11264
	ds_read_b64_tr_b16 v[240:241], v70 offset:11776
	ds_read_b64_tr_b16 v[242:243], v70 offset:15360
	ds_read_b64_tr_b16 v[244:245], v70 offset:15872
	s_waitcnt lgkmcnt(6)
	v_mfma_f32_32x32x16_bf16 v[34:49], v[230:233], v[84:87], v[34:49]
	s_waitcnt lgkmcnt(4)
	v_mfma_f32_32x32x16_bf16 v[18:33], v[234:237], v[84:87], v[18:33]
	ds_read_b64_tr_b16 v[230:231], v70 offset:24576
	ds_read_b64_tr_b16 v[232:233], v70 offset:25088
	ds_read_b64_tr_b16 v[234:235], v70 offset:28672
	ds_read_b64_tr_b16 v[236:237], v70 offset:29184
	s_waitcnt lgkmcnt(6)
	v_mfma_f32_32x32x16_bf16 v[34:49], v[238:241], v[4:7], v[34:49]
	v_cvt_pk_bf16_f32 v76, v8, v9
	v_cvt_pk_bf16_f32 v77, v10, v11
	v_cvt_pk_bf16_f32 v79, v14, v15
	v_cvt_pk_bf16_f32 v14, v50, v51
	v_cvt_pk_bf16_f32 v8, v54, v55
	v_cvt_pk_bf16_f32 v9, v52, v53
	v_cvt_pk_bf16_f32 v11, v56, v57
	s_waitcnt lgkmcnt(4)
	v_mfma_f32_32x32x16_bf16 v[18:33], v[242:245], v[4:7], v[18:33]
	ds_read_b64_tr_b16 v[238:239], v70 offset:25600
	ds_read_b64_tr_b16 v[240:241], v70 offset:26112
	ds_read_b64_tr_b16 v[242:243], v70 offset:29696
	ds_read_b64_tr_b16 v[244:245], v70 offset:30208
	v_cvt_pk_bf16_f32 v78, v12, v13
	v_cvt_pk_bf16_f32 v12, v16, v17
	v_cvt_pk_bf16_f32 v13, v64, v65
	v_cvt_pk_bf16_f32 v15, v74, v75
	v_cvt_pk_bf16_f32 v10, v58, v59
	v_cvt_pk_bf16_f32 v4, v62, v63
	s_waitcnt lgkmcnt(6)
	v_mfma_f32_32x32x16_bf16 v[34:49], v[230:233], v[76:79], v[34:49]
	v_cvt_pk_bf16_f32 v5, v60, v61
	v_cvt_pk_bf16_f32 v6, v72, v73
	v_cvt_pk_bf16_f32 v7, v66, v67
	s_waitcnt lgkmcnt(4)
	v_mfma_f32_32x32x16_bf16 v[18:33], v[234:237], v[76:79], v[18:33]
	ds_read_b64_tr_b16 v[230:231], v70 offset:26624
	ds_read_b64_tr_b16 v[232:233], v70 offset:27136
	ds_read_b64_tr_b16 v[234:235], v70 offset:30720
	ds_read_b64_tr_b16 v[236:237], v70 offset:31232
	s_waitcnt lgkmcnt(6)
	v_mfma_f32_32x32x16_bf16 v[34:49], v[238:241], v[12:15], v[34:49]
	s_waitcnt lgkmcnt(4)
	v_mfma_f32_32x32x16_bf16 v[18:33], v[242:245], v[12:15], v[18:33]
	ds_read_b64_tr_b16 v[238:239], v70 offset:27648
	ds_read_b64_tr_b16 v[240:241], v70 offset:28160
	ds_read_b64_tr_b16 v[242:243], v70 offset:31744
	ds_read_b64_tr_b16 v[244:245], v70 offset:32256
	s_waitcnt lgkmcnt(6)
	v_mfma_f32_32x32x16_bf16 v[34:49], v[230:233], v[8:11], v[34:49]
	s_waitcnt lgkmcnt(4)
	v_mfma_f32_32x32x16_bf16 v[18:33], v[234:237], v[8:11], v[18:33]
	s_waitcnt lgkmcnt(2)
	v_mfma_f32_32x32x16_bf16 v[34:49], v[238:241], v[4:7], v[34:49]
	s_waitcnt lgkmcnt(0)
	v_mfma_f32_32x32x16_bf16 v[18:33], v[242:245], v[4:7], v[18:33]
	s_cbranch_scc1 .LBB0_640
	s_cmp_gt_u32 s78, 7
	s_cselect_b64 s[94:95], -1, 0
	s_cmp_gt_u32 s82, 3
	s_cselect_b64 s[96:97], -1, 0
	s_sub_i32 s0, 3, s80
	s_mov_b32 s1, s16
	s_lshl_b64 s[0:1], s[0:1], 13
	v_readlane_b32 s9, v251, 59
	s_add_u32 s2, s9, s0
	v_readlane_b32 s10, v251, 61
	s_addc_u32 s3, s10, s1
	s_add_i32 s0, s79, 4
	s_mov_b32 s1, s16
	s_lshl_b64 s[0:1], s[0:1], 13
	v_writelane_b32 v249, s40, 10
	s_add_u32 s7, s92, s0
	s_mov_b32 s12, s16
	s_addc_u32 s8, s93, s1
	s_mov_b32 s1, s16
	v_writelane_b32 v249, s12, 11
	s_cmp_gt_u32 s82, 4
	s_cselect_b64 s[4:5], -1, 0
	v_writelane_b32 v249, s13, 12
	s_sub_i32 s0, 4, s80
	v_writelane_b32 v249, s14, 13
	s_lshl_b64 s[0:1], s[0:1], 13
	v_writelane_b32 v249, s15, 14
	s_add_u32 s9, s9, s0
	v_writelane_b32 v249, s16, 15
	s_addc_u32 s10, s10, s1
	s_add_i32 s0, s79, 5
	v_writelane_b32 v249, s17, 16
	s_mov_b32 s1, s16
	v_writelane_b32 v249, s18, 17
	s_lshl_b64 s[0:1], s[0:1], 13
	v_writelane_b32 v249, s19, 18
	s_add_u32 s0, s92, s0
	v_writelane_b32 v249, s20, 19
	s_addc_u32 s1, s93, s1
	s_sub_i32 s11, 30, s6
	v_writelane_b32 v249, s21, 20
	s_cmp_gt_i32 s80, 3
	v_writelane_b32 v249, s22, 21
	s_cselect_b32 s2, s7, s2
	v_writelane_b32 v249, s23, 22
	s_cselect_b32 s3, s8, s3
	s_add_u32 s2, s2, s90
	v_writelane_b32 v249, s24, 23
	s_addc_u32 s3, s3, s91
	v_writelane_b32 v249, s25, 24
	s_cmp_gt_i32 s80, 4
	v_writelane_b32 v249, s26, 25
	s_cselect_b32 s0, s0, s9
	v_writelane_b32 v249, s27, 26
	s_cselect_b32 s1, s1, s10
	s_add_u32 s12, s0, s90
	s_addc_u32 s13, s1, s91
	v_cmp_eq_u32_e32 vcc, 0, v198
	v_cmp_eq_u32_e64 s[0:1], s78, v198
	s_or_b64 s[0:1], vcc, s[0:1]
	v_cmp_eq_u32_e32 vcc, s11, v198
	s_or_b64 s[8:9], s[0:1], vcc
	v_readlane_b32 s0, v250, 44
	v_and_b32_e32 v4, 0x3fffffe0, v68
	v_lshl_add_u64 v[186:187], s[2:3], 0, v[184:185]
	v_lshl_add_u32 v206, v68, 2, s0
	v_lshl_add_u32 v207, v4, 2, s0
	s_mov_b64 s[0:1], 0x800000
	v_lshl_add_u64 v[190:191], s[12:13], 0, v[184:185]
	v_sub_u32_e32 v208, v71, v69
	v_lshl_add_u64 v[188:189], v[186:187], 0, s[0:1]
	v_lshl_add_u64 v[192:193], v[190:191], 0, s[0:1]
	v_mul_lo_u32 v3, v3, s64
	v_lshlrev_b32_e32 v4, 2, v198
	v_readlane_b32 s0, v250, 47
	v_lshlrev_b32_e32 v50, 2, v71
	v_mov_b32_e32 v16, v2
	v_add3_u32 v209, s0, v3, v4
	v_cmp_gt_i32_e64 s[0:1], 1, v208
	v_mov_b32_e32 v17, v2
	s_sub_i32 s83, s80, s6
	v_writelane_b32 v249, s0, 27
	v_mov_b32_e32 v3, v2
	v_mov_b32_e32 v4, v2
	v_writelane_b32 v249, s1, 28
	v_cmp_gt_i32_e64 s[0:1], 0, v208
	v_mov_b32_e32 v5, v2
	v_mov_b32_e32 v6, v2
	v_writelane_b32 v249, s0, 29
	v_mov_b32_e32 v7, v2
	v_mov_b32_e32 v8, v2
	v_writelane_b32 v249, s1, 30
	v_cmp_gt_i32_e64 s[0:1], 33, v208
	v_mov_b32_e32 v9, v2
	v_mov_b32_e32 v10, v2
	v_writelane_b32 v249, s0, 31
	v_mov_b32_e32 v11, v2
	v_mov_b32_e32 v12, v2
	v_writelane_b32 v249, s1, 32
	v_cmp_gt_i32_e64 s[0:1], 32, v208
	v_mov_b32_e32 v13, v2
	v_mov_b32_e32 v14, v2
	v_writelane_b32 v249, s0, 33
	v_mov_b32_e32 v15, v2
	v_add_u32_e32 v50, 0, v50
	v_writelane_b32 v249, s1, 34
	v_cmp_gt_i32_e64 s[0:1], 3, v208
	v_mov_b64_e32 v[96:97], v[16:17]
	v_mov_b64_e32 v[112:113], v[16:17]
	v_writelane_b32 v249, s0, 35
	s_add_i32 s83, s83, 32
	v_cmp_lt_u32_e64 s[6:7], s78, v198
	v_writelane_b32 v249, s1, 36
	v_cmp_gt_i32_e64 s[0:1], 2, v208
	v_mov_b32_e32 v211, 0
	v_cmp_eq_u32_e64 s[10:11], 0, v68
	v_writelane_b32 v249, s0, 37
	v_cmp_ne_u32_e64 s[12:13], 0, v198
	v_cmp_lt_u32_e64 s[14:15], 1, v198
	v_writelane_b32 v249, s1, 38
	v_cmp_gt_i32_e64 s[0:1], 35, v208
	v_cmp_lt_u32_e64 s[16:17], 2, v198
	v_cmp_lt_u32_e64 s[18:19], 3, v198
	v_writelane_b32 v249, s0, 39
	v_cmp_lt_u32_e64 s[20:21], 4, v198
	v_cmp_lt_u32_e64 s[22:23], 5, v198
	v_writelane_b32 v249, s1, 40
	v_cmp_gt_i32_e64 s[0:1], 34, v208
	v_cmp_lt_u32_e64 s[24:25], 6, v198
	v_cmp_lt_u32_e64 s[26:27], 7, v198
	v_writelane_b32 v249, s0, 41
	v_cmp_lt_u32_e64 s[28:29], 8, v198
	v_cmp_lt_u32_e64 s[30:31], 9, v198
	v_writelane_b32 v249, s1, 42
	v_cmp_gt_i32_e64 s[0:1], 9, v208
	v_cmp_lt_u32_e64 s[34:35], 10, v198
	v_cmp_lt_u32_e64 s[36:37], 11, v198
	v_writelane_b32 v249, s0, 43
	v_cmp_lt_u32_e64 s[38:39], 12, v198
	v_cmp_lt_u32_e64 s[40:41], 13, v198
	v_writelane_b32 v249, s1, 44
	v_cmp_gt_i32_e64 s[0:1], 8, v208
	v_cmp_lt_u32_e64 s[42:43], 14, v198
	v_cmp_lt_u32_e64 s[44:45], 15, v198
	v_writelane_b32 v249, s0, 45
	v_cmp_lt_u32_e64 s[46:47], 16, v198
	v_cmp_lt_u32_e64 s[48:49], 17, v198
	v_writelane_b32 v249, s1, 46
	v_cmp_gt_i32_e64 s[0:1], 41, v208
	v_cmp_lt_u32_e64 s[50:51], 18, v198
	v_cmp_lt_u32_e64 s[52:53], 19, v198
	v_writelane_b32 v249, s0, 47
	v_cmp_lt_u32_e64 s[54:55], 20, v198
	v_cmp_lt_u32_e64 s[56:57], 21, v198
	v_writelane_b32 v249, s1, 48
	v_cmp_gt_i32_e64 s[0:1], 40, v208
	v_cmp_lt_u32_e64 s[58:59], 22, v198
	v_cmp_lt_u32_e64 s[60:61], 23, v198
	v_writelane_b32 v249, s0, 49
	v_cmp_lt_u32_e64 s[62:63], 24, v198
	s_mov_b32 s2, 0
	v_writelane_b32 v249, s1, 50
	v_cmp_gt_i32_e64 s[0:1], 11, v208
	v_mov_b32_e32 v214, 0
	v_add_u32_e32 v210, 0x20400, v50
	v_writelane_b32 v249, s0, 51
	v_mov_b32_e32 v114, 0
	v_mov_b64_e32 v[94:95], v[14:15]
	v_writelane_b32 v249, s1, 52
	v_cmp_gt_i32_e64 s[0:1], 10, v208
	v_mov_b64_e32 v[92:93], v[12:13]
	v_mov_b64_e32 v[90:91], v[10:11]
	v_writelane_b32 v249, s0, 53
	v_mov_b64_e32 v[88:89], v[8:9]
	v_mov_b64_e32 v[86:87], v[6:7]
	v_writelane_b32 v249, s1, 54
	v_cmp_gt_i32_e64 s[0:1], 43, v208
	v_mov_b64_e32 v[84:85], v[4:5]
	v_mov_b64_e32 v[82:83], v[2:3]
	v_writelane_b32 v249, s0, 55
	v_mov_b64_e32 v[110:111], v[14:15]
	v_mov_b64_e32 v[108:109], v[12:13]
	v_writelane_b32 v249, s1, 56
	v_cmp_gt_i32_e64 s[0:1], 42, v208
	v_mov_b64_e32 v[106:107], v[10:11]
	v_mov_b64_e32 v[104:105], v[8:9]
	v_writelane_b32 v249, s0, 57
	v_mov_b64_e32 v[102:103], v[6:7]
	v_mov_b64_e32 v[100:101], v[4:5]
	v_writelane_b32 v249, s1, 58
	v_cmp_gt_i32_e64 s[0:1], 17, v208
	v_mov_b64_e32 v[98:99], v[2:3]
	v_cmp_lt_u32_e64 s[64:65], 25, v198
	v_writelane_b32 v249, s0, 59
	v_cmp_lt_u32_e64 s[66:67], 26, v198
	v_cmp_lt_u32_e64 s[68:69], 27, v198
	v_writelane_b32 v249, s1, 60
	v_cmp_gt_i32_e64 s[0:1], 16, v208
	v_cmp_lt_u32_e64 s[70:71], 28, v198
	v_cmp_lt_u32_e64 s[72:73], 29, v198
	v_writelane_b32 v249, s0, 61
	v_cmp_eq_u32_e64 s[74:75], 31, v198
	s_nop 0
	v_writelane_b32 v249, s1, 62
	v_cmp_gt_i32_e64 s[0:1], 49, v208
	s_nop 1
	v_writelane_b32 v249, s0, 63
	s_nop 1
	v_writelane_b32 v248, s1, 0
	v_cmp_gt_i32_e64 s[0:1], 48, v208
	s_nop 1
	v_writelane_b32 v248, s0, 1
	s_nop 1
	v_writelane_b32 v248, s1, 2
	v_cmp_gt_i32_e64 s[0:1], 19, v208
	s_nop 1
	v_writelane_b32 v248, s0, 3
	s_nop 1
	v_writelane_b32 v248, s1, 4
	v_cmp_gt_i32_e64 s[0:1], 18, v208
	s_nop 1
	v_writelane_b32 v248, s0, 5
	s_nop 1
	v_writelane_b32 v248, s1, 6
	v_cmp_gt_i32_e64 s[0:1], 51, v208
	s_nop 1
	v_writelane_b32 v248, s0, 7
	s_nop 1
	v_writelane_b32 v248, s1, 8
	v_cmp_gt_i32_e64 s[0:1], 50, v208
	s_nop 1
	v_writelane_b32 v248, s0, 9
	s_nop 1
	v_writelane_b32 v248, s1, 10
	v_cmp_gt_i32_e64 s[0:1], 25, v208
	s_nop 1
	v_writelane_b32 v248, s0, 11
	s_nop 1
	v_writelane_b32 v248, s1, 12
	v_cmp_gt_i32_e64 s[0:1], 24, v208
	s_nop 1
	v_writelane_b32 v248, s0, 13
	s_nop 1
	v_writelane_b32 v248, s1, 14
	v_cmp_gt_i32_e64 s[0:1], 57, v208
	s_nop 1
	v_writelane_b32 v248, s0, 15
	s_nop 1
	v_writelane_b32 v248, s1, 16
	v_cmp_gt_i32_e64 s[0:1], 56, v208
	s_nop 1
	v_writelane_b32 v248, s0, 17
	s_nop 1
	v_writelane_b32 v248, s1, 18
	v_cmp_gt_i32_e64 s[0:1], 27, v208
	s_nop 1
	v_writelane_b32 v248, s0, 19
	s_nop 1
	v_writelane_b32 v248, s1, 20
	v_cmp_gt_i32_e64 s[0:1], 26, v208
	s_nop 1
	v_writelane_b32 v248, s0, 21
	s_nop 1
	v_writelane_b32 v248, s1, 22
	v_cmp_gt_i32_e64 s[0:1], 59, v208
	s_nop 1
	v_writelane_b32 v248, s0, 23
	s_nop 1
	v_writelane_b32 v248, s1, 24
	v_cmp_gt_i32_e64 s[0:1], 58, v208
	s_nop 1
	v_writelane_b32 v248, s0, 25
	s_nop 1
	v_writelane_b32 v248, s1, 26
	v_mov_b64_e32 v[50:51], 0
	v_mov_b64_e32 v[52:53], 0
	v_mov_b64_e32 v[54:55], 0
	v_mov_b64_e32 v[56:57], 0
	v_mov_b64_e32 v[58:59], 0
	v_mov_b64_e32 v[60:61], 0
	v_mov_b64_e32 v[62:63], 0
	v_mov_b64_e32 v[64:65], 0
	v_mov_b64_e32 v[66:67], 0
	v_mov_b64_e32 v[68:69], 0
	v_mov_b64_e32 v[70:71], 0
	v_mov_b64_e32 v[72:73], 0
	v_mov_b64_e32 v[74:75], 0
	v_mov_b64_e32 v[76:77], 0
	v_mov_b64_e32 v[78:79], 0
	v_mov_b64_e32 v[80:81], 0
	s_mov_b32 s32, 0x8000
	v_readlane_b32 s98, v251, 57
	s_add_i32 s99, s82, -5
	s_max_i32 s99, s99, 0
	s_cmp_gt_i32 s80, 5
	s_cbranch_scc1 .Lnsa_e6_win
	s_sub_i32 s0, 5, s80
	s_lshl_b32 s0, s0, 13
	v_readlane_b32 s100, v251, 59
	v_readlane_b32 s101, v251, 61
	s_branch .Lnsa_e6_done
